# out-projection layer-1 epilogue: residual loads issued together with a single wait (was 2 loads, wait, 14 loads)
# speedup vs baseline: 1.0084x; 1.0084x over previous
.LBB0_667:
	global_load_dwordx4 v[196:199], v[218:219], off
	global_load_dwordx4 v[186:189], v[218:219], off offset:256
	v_add_co_u32_e32 v232, vcc, 0x8000, v218
	s_nop 0
	s_nop 0
	v_addc_co_u32_e32 v233, vcc, 0, v219, vcc
	global_load_dwordx4 v[182:185], v[232:233], off
	global_load_dwordx4 v[178:181], v[232:233], off offset:256
	v_add_co_u32_e32 v230, vcc, 0x10000, v218
	s_nop 0
	s_nop 0
	v_addc_co_u32_e32 v231, vcc, 0, v219, vcc
	global_load_dwordx4 v[174:177], v[230:231], off
	global_load_dwordx4 v[170:173], v[230:231], off offset:256
	v_add_co_u32_e32 v228, vcc, 0x18000, v218
	s_nop 0
	s_nop 0
	v_addc_co_u32_e32 v229, vcc, 0, v219, vcc
	global_load_dwordx4 v[166:169], v[228:229], off
	global_load_dwordx4 v[162:165], v[228:229], off offset:256
	v_add_co_u32_e32 v226, vcc, 0x40000, v218
	s_nop 0
	s_nop 0
	v_addc_co_u32_e32 v227, vcc, 0, v219, vcc
	global_load_dwordx4 v[158:161], v[226:227], off
	global_load_dwordx4 v[154:157], v[226:227], off offset:256
	v_add_co_u32_e32 v224, vcc, 0x48000, v218
	s_nop 0
	s_nop 0
	v_addc_co_u32_e32 v225, vcc, 0, v219, vcc
	global_load_dwordx4 v[150:153], v[224:225], off
	global_load_dwordx4 v[146:149], v[224:225], off offset:256
	v_add_co_u32_e32 v222, vcc, 0x50000, v218
	s_nop 0
	s_nop 0
	v_addc_co_u32_e32 v223, vcc, 0, v219, vcc
	global_load_dwordx4 v[142:145], v[222:223], off
	global_load_dwordx4 v[138:141], v[222:223], off offset:256
	v_add_co_u32_e32 v220, vcc, 0x58000, v218
	s_nop 0
	s_nop 0
	v_addc_co_u32_e32 v221, vcc, 0, v219, vcc
	global_load_dwordx4 v[134:137], v[220:221], off
	global_load_dwordx4 v[130:133], v[220:221], off offset:256
	s_waitcnt vmcnt(0)
	v_lshlrev_b32_e32 v200, 16, v196
	v_and_b32_e32 v201, 0xffff0000, v196
	v_lshlrev_b32_e32 v196, 16, v197
	v_and_b32_e32 v197, 0xffff0000, v197
	v_lshlrev_b32_e32 v202, 16, v198
	v_and_b32_e32 v203, 0xffff0000, v198
	v_lshlrev_b32_e32 v198, 16, v199
	v_and_b32_e32 v199, 0xffff0000, v199
	v_pk_add_f32 v[128:129], v[128:129], v[196:197]
	v_pk_add_f32 v[126:127], v[126:127], v[200:201]
	v_pk_add_f32 v[196:197], v[124:125], v[198:199]
	v_pk_add_f32 v[124:125], v[122:123], v[202:203]
	v_cvt_pk_bf16_f32 v122, v126, v127
	v_cvt_pk_bf16_f32 v123, v128, v129
	v_lshlrev_b32_e32 v126, 16, v188
	v_cvt_pk_bf16_f32 v124, v124, v125
	v_cvt_pk_bf16_f32 v125, v196, v197
	global_store_dwordx4 v[218:219], v[122:125], off
	v_and_b32_e32 v127, 0xffff0000, v188
	v_lshlrev_b32_e32 v128, 16, v189
	v_lshlrev_b32_e32 v122, 16, v186
	v_and_b32_e32 v123, 0xffff0000, v186
	v_and_b32_e32 v129, 0xffff0000, v189
	v_lshlrev_b32_e32 v124, 16, v187
	v_and_b32_e32 v125, 0xffff0000, v187
	v_pk_add_f32 v[118:119], v[118:119], v[122:123]
	v_pk_add_f32 v[122:123], v[116:117], v[128:129]
	v_pk_add_f32 v[116:117], v[114:115], v[126:127]
	v_pk_add_f32 v[120:121], v[120:121], v[124:125]
	v_cvt_pk_bf16_f32 v114, v118, v119
	s_waitcnt vmcnt(0)
	v_lshlrev_b32_e32 v118, 16, v184
	v_cvt_pk_bf16_f32 v115, v120, v121
	v_cvt_pk_bf16_f32 v116, v116, v117
	v_cvt_pk_bf16_f32 v117, v122, v123
	global_store_dwordx4 v[218:219], v[114:117], off offset:256
	v_and_b32_e32 v119, 0xffff0000, v184
	v_lshlrev_b32_e32 v120, 16, v185
	v_lshlrev_b32_e32 v114, 16, v182
	v_and_b32_e32 v115, 0xffff0000, v182
	v_lshlrev_b32_e32 v116, 16, v183
	v_and_b32_e32 v117, 0xffff0000, v183
	v_and_b32_e32 v121, 0xffff0000, v185
	v_pk_add_f32 v[112:113], v[112:113], v[116:117]
	v_pk_add_f32 v[110:111], v[110:111], v[114:115]
	v_pk_add_f32 v[114:115], v[108:109], v[120:121]
	v_pk_add_f32 v[108:109], v[106:107], v[118:119]
	v_cvt_pk_bf16_f32 v106, v110, v111
	v_cvt_pk_bf16_f32 v107, v112, v113
	v_lshlrev_b32_e32 v110, 16, v180
	v_cvt_pk_bf16_f32 v108, v108, v109
	v_cvt_pk_bf16_f32 v109, v114, v115
	global_store_dwordx4 v[232:233], v[106:109], off
	v_and_b32_e32 v111, 0xffff0000, v180
	v_lshlrev_b32_e32 v112, 16, v181
	v_lshlrev_b32_e32 v106, 16, v178
	v_and_b32_e32 v107, 0xffff0000, v178
	v_and_b32_e32 v113, 0xffff0000, v181
	v_lshlrev_b32_e32 v108, 16, v179
	v_and_b32_e32 v109, 0xffff0000, v179
	v_pk_add_f32 v[102:103], v[102:103], v[106:107]
	v_pk_add_f32 v[106:107], v[100:101], v[112:113]
	v_pk_add_f32 v[100:101], v[98:99], v[110:111]
	v_pk_add_f32 v[104:105], v[104:105], v[108:109]
	v_cvt_pk_bf16_f32 v98, v102, v103
	v_lshlrev_b32_e32 v102, 16, v176
	v_cvt_pk_bf16_f32 v99, v104, v105
	v_cvt_pk_bf16_f32 v100, v100, v101
	v_cvt_pk_bf16_f32 v101, v106, v107
	global_store_dwordx4 v[232:233], v[98:101], off offset:256
	v_and_b32_e32 v103, 0xffff0000, v176
	v_lshlrev_b32_e32 v104, 16, v177
	v_lshlrev_b32_e32 v98, 16, v174
	v_and_b32_e32 v99, 0xffff0000, v174
	v_lshlrev_b32_e32 v100, 16, v175
	v_and_b32_e32 v101, 0xffff0000, v175
	v_and_b32_e32 v105, 0xffff0000, v177
	v_pk_add_f32 v[96:97], v[96:97], v[100:101]
	v_pk_add_f32 v[94:95], v[94:95], v[98:99]
	v_pk_add_f32 v[98:99], v[92:93], v[104:105]
	v_pk_add_f32 v[92:93], v[90:91], v[102:103]
	v_cvt_pk_bf16_f32 v90, v94, v95
	v_cvt_pk_bf16_f32 v91, v96, v97
	v_lshlrev_b32_e32 v94, 16, v172
	v_cvt_pk_bf16_f32 v92, v92, v93
	v_cvt_pk_bf16_f32 v93, v98, v99
	global_store_dwordx4 v[230:231], v[90:93], off
	v_and_b32_e32 v95, 0xffff0000, v172
	v_lshlrev_b32_e32 v96, 16, v173
	v_lshlrev_b32_e32 v90, 16, v170
	v_and_b32_e32 v91, 0xffff0000, v170
	v_and_b32_e32 v97, 0xffff0000, v173
	v_lshlrev_b32_e32 v92, 16, v171
	v_and_b32_e32 v93, 0xffff0000, v171
	v_pk_add_f32 v[86:87], v[86:87], v[90:91]
	v_pk_add_f32 v[90:91], v[84:85], v[96:97]
	v_pk_add_f32 v[84:85], v[82:83], v[94:95]
	v_pk_add_f32 v[88:89], v[88:89], v[92:93]
	v_cvt_pk_bf16_f32 v82, v86, v87
	v_lshlrev_b32_e32 v86, 16, v168
	v_cvt_pk_bf16_f32 v83, v88, v89
	v_cvt_pk_bf16_f32 v84, v84, v85
	v_cvt_pk_bf16_f32 v85, v90, v91
	global_store_dwordx4 v[230:231], v[82:85], off offset:256
	v_and_b32_e32 v87, 0xffff0000, v168
	v_lshlrev_b32_e32 v88, 16, v169
	v_lshlrev_b32_e32 v82, 16, v166
	v_and_b32_e32 v83, 0xffff0000, v166
	v_lshlrev_b32_e32 v84, 16, v167
	v_and_b32_e32 v85, 0xffff0000, v167
	v_and_b32_e32 v89, 0xffff0000, v169
	v_pk_add_f32 v[80:81], v[80:81], v[84:85]
	v_pk_add_f32 v[78:79], v[78:79], v[82:83]
	v_pk_add_f32 v[82:83], v[76:77], v[88:89]
	v_pk_add_f32 v[76:77], v[74:75], v[86:87]
	v_cvt_pk_bf16_f32 v74, v78, v79
	v_cvt_pk_bf16_f32 v75, v80, v81
	v_lshlrev_b32_e32 v78, 16, v164
	v_cvt_pk_bf16_f32 v76, v76, v77
	v_cvt_pk_bf16_f32 v77, v82, v83
	global_store_dwordx4 v[228:229], v[74:77], off
	v_and_b32_e32 v79, 0xffff0000, v164
	v_lshlrev_b32_e32 v80, 16, v165
	v_lshlrev_b32_e32 v74, 16, v162
	v_and_b32_e32 v75, 0xffff0000, v162
	v_and_b32_e32 v81, 0xffff0000, v165
	v_lshlrev_b32_e32 v76, 16, v163
	v_and_b32_e32 v77, 0xffff0000, v163
	v_pk_add_f32 v[70:71], v[70:71], v[74:75]
	v_pk_add_f32 v[74:75], v[68:69], v[80:81]
	v_pk_add_f32 v[68:69], v[66:67], v[78:79]
	v_pk_add_f32 v[72:73], v[72:73], v[76:77]
	v_cvt_pk_bf16_f32 v66, v70, v71
	v_lshlrev_b32_e32 v70, 16, v160
	v_cvt_pk_bf16_f32 v67, v72, v73
	v_cvt_pk_bf16_f32 v68, v68, v69
	v_cvt_pk_bf16_f32 v69, v74, v75
	global_store_dwordx4 v[228:229], v[66:69], off offset:256
	v_and_b32_e32 v71, 0xffff0000, v160
	v_lshlrev_b32_e32 v72, 16, v161
	v_lshlrev_b32_e32 v66, 16, v158
	v_and_b32_e32 v67, 0xffff0000, v158
	v_lshlrev_b32_e32 v68, 16, v159
	v_and_b32_e32 v69, 0xffff0000, v159
	v_and_b32_e32 v73, 0xffff0000, v161
	v_pk_add_f32 v[64:65], v[64:65], v[68:69]
	v_pk_add_f32 v[62:63], v[62:63], v[66:67]
	v_pk_add_f32 v[66:67], v[60:61], v[72:73]
	v_pk_add_f32 v[60:61], v[58:59], v[70:71]
	v_cvt_pk_bf16_f32 v58, v62, v63
	v_cvt_pk_bf16_f32 v59, v64, v65
	v_lshlrev_b32_e32 v62, 16, v156
	v_cvt_pk_bf16_f32 v60, v60, v61
	v_cvt_pk_bf16_f32 v61, v66, v67
	global_store_dwordx4 v[226:227], v[58:61], off
	v_and_b32_e32 v63, 0xffff0000, v156
	v_lshlrev_b32_e32 v64, 16, v157
	v_lshlrev_b32_e32 v58, 16, v154
	v_and_b32_e32 v59, 0xffff0000, v154
	v_and_b32_e32 v65, 0xffff0000, v157
	v_lshlrev_b32_e32 v60, 16, v155
	v_and_b32_e32 v61, 0xffff0000, v155
	v_pk_add_f32 v[54:55], v[54:55], v[58:59]
	v_pk_add_f32 v[58:59], v[52:53], v[64:65]
	v_pk_add_f32 v[52:53], v[50:51], v[62:63]
	v_pk_add_f32 v[56:57], v[56:57], v[60:61]
	v_cvt_pk_bf16_f32 v50, v54, v55
	v_lshlrev_b32_e32 v54, 16, v152
	v_cvt_pk_bf16_f32 v51, v56, v57
	v_cvt_pk_bf16_f32 v52, v52, v53
	v_cvt_pk_bf16_f32 v53, v58, v59
	global_store_dwordx4 v[226:227], v[50:53], off offset:256
	v_and_b32_e32 v55, 0xffff0000, v152
	v_lshlrev_b32_e32 v56, 16, v153
	v_lshlrev_b32_e32 v50, 16, v150
	v_and_b32_e32 v51, 0xffff0000, v150
	v_lshlrev_b32_e32 v52, 16, v151
	v_and_b32_e32 v53, 0xffff0000, v151
	v_and_b32_e32 v57, 0xffff0000, v153
	v_pk_add_f32 v[48:49], v[48:49], v[52:53]
	v_pk_add_f32 v[46:47], v[46:47], v[50:51]
	v_pk_add_f32 v[50:51], v[44:45], v[56:57]
	v_pk_add_f32 v[44:45], v[42:43], v[54:55]
	v_cvt_pk_bf16_f32 v42, v46, v47
	v_cvt_pk_bf16_f32 v43, v48, v49
	v_lshlrev_b32_e32 v46, 16, v148
	v_cvt_pk_bf16_f32 v44, v44, v45
	v_cvt_pk_bf16_f32 v45, v50, v51
	global_store_dwordx4 v[224:225], v[42:45], off
	v_and_b32_e32 v47, 0xffff0000, v148
	v_lshlrev_b32_e32 v48, 16, v149
	v_lshlrev_b32_e32 v42, 16, v146
	v_and_b32_e32 v43, 0xffff0000, v146
	v_and_b32_e32 v49, 0xffff0000, v149
	v_lshlrev_b32_e32 v44, 16, v147
	v_and_b32_e32 v45, 0xffff0000, v147
	v_pk_add_f32 v[38:39], v[38:39], v[42:43]
	v_pk_add_f32 v[42:43], v[36:37], v[48:49]
	v_pk_add_f32 v[36:37], v[34:35], v[46:47]
	v_pk_add_f32 v[40:41], v[40:41], v[44:45]
	v_cvt_pk_bf16_f32 v34, v38, v39
	v_lshlrev_b32_e32 v38, 16, v144
	v_cvt_pk_bf16_f32 v35, v40, v41
	v_cvt_pk_bf16_f32 v36, v36, v37
	v_cvt_pk_bf16_f32 v37, v42, v43
	global_store_dwordx4 v[224:225], v[34:37], off offset:256
	v_and_b32_e32 v39, 0xffff0000, v144
	v_lshlrev_b32_e32 v40, 16, v145
	v_lshlrev_b32_e32 v34, 16, v142
	v_and_b32_e32 v35, 0xffff0000, v142
	v_lshlrev_b32_e32 v36, 16, v143
	v_and_b32_e32 v37, 0xffff0000, v143
	v_and_b32_e32 v41, 0xffff0000, v145
	v_pk_add_f32 v[32:33], v[32:33], v[36:37]
	v_pk_add_f32 v[30:31], v[30:31], v[34:35]
	v_pk_add_f32 v[34:35], v[28:29], v[40:41]
	v_pk_add_f32 v[28:29], v[26:27], v[38:39]
	v_cvt_pk_bf16_f32 v26, v30, v31
	v_cvt_pk_bf16_f32 v27, v32, v33
	v_lshlrev_b32_e32 v30, 16, v140
	v_cvt_pk_bf16_f32 v28, v28, v29
	v_cvt_pk_bf16_f32 v29, v34, v35
	global_store_dwordx4 v[222:223], v[26:29], off
	v_and_b32_e32 v31, 0xffff0000, v140
	v_lshlrev_b32_e32 v32, 16, v141
	v_lshlrev_b32_e32 v26, 16, v138
	v_and_b32_e32 v27, 0xffff0000, v138
	v_and_b32_e32 v33, 0xffff0000, v141
	v_lshlrev_b32_e32 v28, 16, v139
	v_and_b32_e32 v29, 0xffff0000, v139
	v_pk_add_f32 v[22:23], v[22:23], v[26:27]
	v_pk_add_f32 v[26:27], v[20:21], v[32:33]
	v_pk_add_f32 v[20:21], v[18:19], v[30:31]
	v_pk_add_f32 v[24:25], v[24:25], v[28:29]
	v_cvt_pk_bf16_f32 v18, v22, v23
	v_lshlrev_b32_e32 v22, 16, v136
	v_cvt_pk_bf16_f32 v19, v24, v25
	v_cvt_pk_bf16_f32 v20, v20, v21
	v_cvt_pk_bf16_f32 v21, v26, v27
	global_store_dwordx4 v[222:223], v[18:21], off offset:256
	v_and_b32_e32 v23, 0xffff0000, v136
	v_lshlrev_b32_e32 v24, 16, v137
	v_lshlrev_b32_e32 v18, 16, v134
	v_and_b32_e32 v19, 0xffff0000, v134
	v_lshlrev_b32_e32 v20, 16, v135
	v_and_b32_e32 v21, 0xffff0000, v135
	v_and_b32_e32 v25, 0xffff0000, v137
	v_pk_add_f32 v[16:17], v[16:17], v[20:21]
	v_pk_add_f32 v[14:15], v[14:15], v[18:19]
	v_pk_add_f32 v[18:19], v[12:13], v[24:25]
	v_pk_add_f32 v[12:13], v[10:11], v[22:23]
	v_cvt_pk_bf16_f32 v10, v14, v15
	v_cvt_pk_bf16_f32 v11, v16, v17
	v_lshlrev_b32_e32 v14, 16, v132
	v_cvt_pk_bf16_f32 v12, v12, v13
	v_cvt_pk_bf16_f32 v13, v18, v19
	global_store_dwordx4 v[220:221], v[10:13], off
	v_and_b32_e32 v15, 0xffff0000, v132
	v_lshlrev_b32_e32 v16, 16, v133
	v_lshlrev_b32_e32 v10, 16, v130
	v_and_b32_e32 v11, 0xffff0000, v130
	v_and_b32_e32 v17, 0xffff0000, v133
	v_lshlrev_b32_e32 v12, 16, v131
	v_and_b32_e32 v13, 0xffff0000, v131
	v_pk_add_f32 v[6:7], v[6:7], v[10:11]
	v_pk_add_f32 v[10:11], v[4:5], v[16:17]
	v_pk_add_f32 v[4:5], v[2:3], v[14:15]
	v_pk_add_f32 v[8:9], v[8:9], v[12:13]
	v_cvt_pk_bf16_f32 v2, v6, v7
	s_nop 0
	v_cvt_pk_bf16_f32 v3, v8, v9
	v_cvt_pk_bf16_f32 v4, v4, v5
	v_cvt_pk_bf16_f32 v5, v10, v11
	global_store_dwordx4 v[220:221], v[2:5], off offset:256
